# P7 EpiGlu epilogue: packed-f32 forms (pk_fma bias/scale, pk_add, pk_mul) instead of scalar mul/add chains
# speedup vs baseline: 1.0038x; 1.0038x over previous
.Lp7_nopf:
	v_mov_b32_e32 v176, 0x41000000
	v_mov_b32_e32 v178, 0xc01d265f
	v_mov_b32_e32 v150, s5
	ds_read_b32 v151, v150
	v_or_b32_e32 v150, s66, v159
	s_waitcnt vmcnt(12)
	s_waitcnt lgkmcnt(0)
	v_subrev_u32_e32 v151, s8, v151
	v_cmp_lt_i32_e32 vcc, v150, v151
	s_and_saveexec_b64 s[0:1], vcc
	s_cbranch_execz .LBB0_967
	v_mul_f32_e32 v174, 0x3a800000, v158
	v_cvt_f32_i32_e32 v138, v138
	v_cvt_f32_i32_e32 v139, v139
	v_cvt_f32_i32_e32 v140, v140
	v_cvt_f32_i32_e32 v141, v141
	v_cvt_f32_i32_e32 v134, v134
	v_cvt_f32_i32_e32 v135, v135
	v_cvt_f32_i32_e32 v136, v136
	v_cvt_f32_i32_e32 v137, v137
	v_cvt_f32_i32_e32 v122, v122
	v_cvt_f32_i32_e32 v123, v123
	v_cvt_f32_i32_e32 v124, v124
	v_cvt_f32_i32_e32 v125, v125
	v_cvt_f32_i32_e32 v118, v118
	v_cvt_f32_i32_e32 v119, v119
	v_cvt_f32_i32_e32 v120, v120
	v_cvt_f32_i32_e32 v121, v121
	v_pk_fma_f32 v[138:139], v[138:139], v[174:175], v[146:147] op_sel_hi:[1,0,1]
	v_pk_fma_f32 v[134:135], v[134:135], v[174:175], v[142:143] op_sel_hi:[1,0,1]
	v_pk_fma_f32 v[140:141], v[140:141], v[174:175], v[148:149] op_sel_hi:[1,0,1]
	v_pk_fma_f32 v[136:137], v[136:137], v[174:175], v[144:145] op_sel_hi:[1,0,1]
	v_pk_fma_f32 v[122:123], v[122:123], v[174:175], v[130:131] op_sel_hi:[1,0,1]
	v_pk_fma_f32 v[118:119], v[118:119], v[174:175], v[126:127] op_sel_hi:[1,0,1]
	v_pk_fma_f32 v[124:125], v[124:125], v[174:175], v[132:133] op_sel_hi:[1,0,1]
	v_pk_fma_f32 v[120:121], v[120:121], v[174:175], v[128:129] op_sel_hi:[1,0,1]
	v_min_f32_e32 v138, 0x40e00000, v138
	v_min_f32_e32 v139, 0x40e00000, v139
	v_min_f32_e32 v140, 0x40e00000, v140
	v_min_f32_e32 v141, 0x40e00000, v141
	v_min_f32_e32 v122, 0x40e00000, v122
	v_min_f32_e32 v123, 0x40e00000, v123
	v_min_f32_e32 v124, 0x40e00000, v124
	v_min_f32_e32 v125, 0x40e00000, v125
	v_pk_mul_f32 v[166:167], v[138:139], v[178:179] op_sel_hi:[1,0]
	v_pk_mul_f32 v[168:169], v[140:141], v[178:179] op_sel_hi:[1,0]
	v_pk_mul_f32 v[170:171], v[122:123], v[178:179] op_sel_hi:[1,0]
	v_pk_mul_f32 v[172:173], v[124:125], v[178:179] op_sel_hi:[1,0]
	v_med3_f32 v134, v134, s74, v223
	v_med3_f32 v135, v135, s74, v223
	v_med3_f32 v136, v136, s74, v223
	v_med3_f32 v137, v137, s74, v223
	v_med3_f32 v118, v118, s74, v223
	v_med3_f32 v119, v119, s74, v223
	v_med3_f32 v120, v120, s74, v223
	v_med3_f32 v121, v121, s74, v223
	v_exp_f32_e32 v166, v166
	v_exp_f32_e32 v167, v167
	v_exp_f32_e32 v168, v168
	v_exp_f32_e32 v169, v169
	v_exp_f32_e32 v170, v170
	v_exp_f32_e32 v171, v171
	v_exp_f32_e32 v172, v172
	v_exp_f32_e32 v173, v173
	v_pk_add_f32 v[134:135], v[134:135], 1.0 op_sel_hi:[1,0]
	v_pk_add_f32 v[136:137], v[136:137], 1.0 op_sel_hi:[1,0]
	v_pk_add_f32 v[118:119], v[118:119], 1.0 op_sel_hi:[1,0]
	v_pk_add_f32 v[120:121], v[120:121], 1.0 op_sel_hi:[1,0]
	v_pk_add_f32 v[166:167], v[166:167], 1.0 op_sel_hi:[1,0]
	v_pk_add_f32 v[168:169], v[168:169], 1.0 op_sel_hi:[1,0]
	v_pk_add_f32 v[170:171], v[170:171], 1.0 op_sel_hi:[1,0]
	v_pk_add_f32 v[172:173], v[172:173], 1.0 op_sel_hi:[1,0]
	v_rcp_f32_e32 v166, v166
	v_rcp_f32_e32 v167, v167
	v_rcp_f32_e32 v168, v168
	v_rcp_f32_e32 v169, v169
	v_rcp_f32_e32 v170, v170
	v_rcp_f32_e32 v171, v171
	v_rcp_f32_e32 v172, v172
	v_rcp_f32_e32 v173, v173
	s_nop 0
	v_pk_mul_f32 v[138:139], v[138:139], v[166:167]
	v_pk_mul_f32 v[140:141], v[140:141], v[168:169]
	v_pk_mul_f32 v[122:123], v[122:123], v[170:171]
	v_pk_mul_f32 v[124:125], v[124:125], v[172:173]
	v_pk_mul_f32 v[134:135], v[134:135], v[138:139]
	v_pk_mul_f32 v[136:137], v[136:137], v[140:141]
	v_pk_mul_f32 v[118:119], v[118:119], v[122:123]
	v_pk_mul_f32 v[120:121], v[120:121], v[124:125]
	v_pk_fma_f32 v[134:135], v[134:135], v[176:177], v[222:223] op_sel_hi:[1,0,0]
	v_pk_fma_f32 v[136:137], v[136:137], v[176:177], v[222:223] op_sel_hi:[1,0,0]
	v_pk_fma_f32 v[118:119], v[118:119], v[176:177], v[222:223] op_sel_hi:[1,0,0]
	v_pk_fma_f32 v[120:121], v[120:121], v[176:177], v[222:223] op_sel_hi:[1,0,0]
	v_med3_f32 v134, v134, s75, v224
	v_med3_f32 v135, v135, s75, v224
	v_med3_f32 v136, v136, s75, v224
	v_med3_f32 v137, v137, s75, v224
	v_med3_f32 v118, v118, s75, v224
	v_med3_f32 v119, v119, s75, v224
	v_med3_f32 v120, v120, s75, v224
	v_med3_f32 v121, v121, s75, v224
	v_perm_b32 v134, v135, v134, s76
	v_perm_b32 v136, v137, v136, s76
	v_perm_b32 v118, v119, v118, s76
	v_perm_b32 v120, v121, v120, s76
	v_perm_b32 v166, v136, v134, s77
	v_perm_b32 v167, v120, v118, s77
	v_add_u32_e32 v118, s4, v150
	v_ashrrev_i32_e32 v119, 31, v118
	v_lshlrev_b64 v[118:119], 11, v[118:119]
	v_lshl_add_u64 v[118:119], s[10:11], 0, v[118:119]
	v_lshl_add_u64 v[118:119], v[118:119], 0, v[4:5]
	v_mov_b32_e32 v134, v166
	v_mov_b32_e32 v135, v167
	global_store_dwordx2 v[118:119], v[134:135], off
.LBB0_967:
	s_or_b64 exec, exec, s[0:1]
	v_or_b32_e32 v118, 16, v150
	v_cmp_lt_i32_e32 vcc, v118, v151
	s_and_saveexec_b64 s[0:1], vcc
	s_cbranch_execz .LBB0_969
	v_mul_f32_e32 v174, 0x3a800000, v157
	v_cvt_f32_i32_e32 v114, v114
	v_cvt_f32_i32_e32 v115, v115
	v_cvt_f32_i32_e32 v116, v116
	v_cvt_f32_i32_e32 v117, v117
	v_cvt_f32_i32_e32 v110, v110
	v_cvt_f32_i32_e32 v111, v111
	v_cvt_f32_i32_e32 v112, v112
	v_cvt_f32_i32_e32 v113, v113
	v_cvt_f32_i32_e32 v106, v106
	v_cvt_f32_i32_e32 v107, v107
	v_cvt_f32_i32_e32 v108, v108
	v_cvt_f32_i32_e32 v109, v109
	v_cvt_f32_i32_e32 v102, v102
	v_cvt_f32_i32_e32 v103, v103
	v_cvt_f32_i32_e32 v104, v104
	v_cvt_f32_i32_e32 v105, v105
	v_pk_fma_f32 v[114:115], v[114:115], v[174:175], v[146:147] op_sel_hi:[1,0,1]
	v_pk_fma_f32 v[110:111], v[110:111], v[174:175], v[142:143] op_sel_hi:[1,0,1]
	v_pk_fma_f32 v[116:117], v[116:117], v[174:175], v[148:149] op_sel_hi:[1,0,1]
	v_pk_fma_f32 v[112:113], v[112:113], v[174:175], v[144:145] op_sel_hi:[1,0,1]
	v_pk_fma_f32 v[106:107], v[106:107], v[174:175], v[130:131] op_sel_hi:[1,0,1]
	v_pk_fma_f32 v[102:103], v[102:103], v[174:175], v[126:127] op_sel_hi:[1,0,1]
	v_pk_fma_f32 v[108:109], v[108:109], v[174:175], v[132:133] op_sel_hi:[1,0,1]
	v_pk_fma_f32 v[104:105], v[104:105], v[174:175], v[128:129] op_sel_hi:[1,0,1]
	v_min_f32_e32 v114, 0x40e00000, v114
	v_min_f32_e32 v115, 0x40e00000, v115
	v_min_f32_e32 v116, 0x40e00000, v116
	v_min_f32_e32 v117, 0x40e00000, v117
	v_min_f32_e32 v106, 0x40e00000, v106
	v_min_f32_e32 v107, 0x40e00000, v107
	v_min_f32_e32 v108, 0x40e00000, v108
	v_min_f32_e32 v109, 0x40e00000, v109
	v_pk_mul_f32 v[166:167], v[114:115], v[178:179] op_sel_hi:[1,0]
	v_pk_mul_f32 v[168:169], v[116:117], v[178:179] op_sel_hi:[1,0]
	v_pk_mul_f32 v[170:171], v[106:107], v[178:179] op_sel_hi:[1,0]
	v_pk_mul_f32 v[172:173], v[108:109], v[178:179] op_sel_hi:[1,0]
	v_med3_f32 v110, v110, s74, v223
	v_med3_f32 v111, v111, s74, v223
	v_med3_f32 v112, v112, s74, v223
	v_med3_f32 v113, v113, s74, v223
	v_med3_f32 v102, v102, s74, v223
	v_med3_f32 v103, v103, s74, v223
	v_med3_f32 v104, v104, s74, v223
	v_med3_f32 v105, v105, s74, v223
	v_exp_f32_e32 v166, v166
	v_exp_f32_e32 v167, v167
	v_exp_f32_e32 v168, v168
	v_exp_f32_e32 v169, v169
	v_exp_f32_e32 v170, v170
	v_exp_f32_e32 v171, v171
	v_exp_f32_e32 v172, v172
	v_exp_f32_e32 v173, v173
	v_pk_add_f32 v[110:111], v[110:111], 1.0 op_sel_hi:[1,0]
	v_pk_add_f32 v[112:113], v[112:113], 1.0 op_sel_hi:[1,0]
	v_pk_add_f32 v[102:103], v[102:103], 1.0 op_sel_hi:[1,0]
	v_pk_add_f32 v[104:105], v[104:105], 1.0 op_sel_hi:[1,0]
	v_pk_add_f32 v[166:167], v[166:167], 1.0 op_sel_hi:[1,0]
	v_pk_add_f32 v[168:169], v[168:169], 1.0 op_sel_hi:[1,0]
	v_pk_add_f32 v[170:171], v[170:171], 1.0 op_sel_hi:[1,0]
	v_pk_add_f32 v[172:173], v[172:173], 1.0 op_sel_hi:[1,0]
	v_rcp_f32_e32 v166, v166
	v_rcp_f32_e32 v167, v167
	v_rcp_f32_e32 v168, v168
	v_rcp_f32_e32 v169, v169
	v_rcp_f32_e32 v170, v170
	v_rcp_f32_e32 v171, v171
	v_rcp_f32_e32 v172, v172
	v_rcp_f32_e32 v173, v173
	s_nop 0
	v_pk_mul_f32 v[114:115], v[114:115], v[166:167]
	v_pk_mul_f32 v[116:117], v[116:117], v[168:169]
	v_pk_mul_f32 v[106:107], v[106:107], v[170:171]
	v_pk_mul_f32 v[108:109], v[108:109], v[172:173]
	v_pk_mul_f32 v[110:111], v[110:111], v[114:115]
	v_pk_mul_f32 v[112:113], v[112:113], v[116:117]
	v_pk_mul_f32 v[102:103], v[102:103], v[106:107]
	v_pk_mul_f32 v[104:105], v[104:105], v[108:109]
	v_pk_fma_f32 v[110:111], v[110:111], v[176:177], v[222:223] op_sel_hi:[1,0,0]
	v_pk_fma_f32 v[112:113], v[112:113], v[176:177], v[222:223] op_sel_hi:[1,0,0]
	v_pk_fma_f32 v[102:103], v[102:103], v[176:177], v[222:223] op_sel_hi:[1,0,0]
	v_pk_fma_f32 v[104:105], v[104:105], v[176:177], v[222:223] op_sel_hi:[1,0,0]
	v_med3_f32 v110, v110, s75, v224
	v_med3_f32 v111, v111, s75, v224
	v_med3_f32 v112, v112, s75, v224
	v_med3_f32 v113, v113, s75, v224
	v_med3_f32 v102, v102, s75, v224
	v_med3_f32 v103, v103, s75, v224
	v_med3_f32 v104, v104, s75, v224
	v_med3_f32 v105, v105, s75, v224
	v_perm_b32 v110, v111, v110, s76
	v_perm_b32 v112, v113, v112, s76
	v_perm_b32 v102, v103, v102, s76
	v_perm_b32 v104, v105, v104, s76
	v_perm_b32 v166, v112, v110, s77
	v_perm_b32 v167, v104, v102, s77
	v_add_u32_e32 v102, s4, v118
	v_ashrrev_i32_e32 v103, 31, v102
	v_lshlrev_b64 v[102:103], 11, v[102:103]
	v_lshl_add_u64 v[102:103], s[10:11], 0, v[102:103]
	v_lshl_add_u64 v[102:103], v[102:103], 0, v[4:5]
	v_mov_b32_e32 v110, v166
	v_mov_b32_e32 v111, v167
	global_store_dwordx2 v[102:103], v[110:111], off
.LBB0_969:
	s_or_b64 exec, exec, s[0:1]
	v_or_b32_e32 v102, 32, v150
	v_cmp_lt_i32_e32 vcc, v102, v151
	s_and_saveexec_b64 s[0:1], vcc
	s_cbranch_execz .LBB0_971
	v_mul_f32_e32 v174, 0x3a800000, v156
	v_cvt_f32_i32_e32 v98, v98
	v_cvt_f32_i32_e32 v99, v99
	v_cvt_f32_i32_e32 v100, v100
	v_cvt_f32_i32_e32 v101, v101
	v_cvt_f32_i32_e32 v94, v94
	v_cvt_f32_i32_e32 v95, v95
	v_cvt_f32_i32_e32 v96, v96
	v_cvt_f32_i32_e32 v97, v97
	v_cvt_f32_i32_e32 v90, v90
	v_cvt_f32_i32_e32 v91, v91
	v_cvt_f32_i32_e32 v92, v92
	v_cvt_f32_i32_e32 v93, v93
	v_cvt_f32_i32_e32 v86, v86
	v_cvt_f32_i32_e32 v87, v87
	v_cvt_f32_i32_e32 v88, v88
	v_cvt_f32_i32_e32 v89, v89
	v_pk_fma_f32 v[98:99], v[98:99], v[174:175], v[146:147] op_sel_hi:[1,0,1]
	v_pk_fma_f32 v[94:95], v[94:95], v[174:175], v[142:143] op_sel_hi:[1,0,1]
	v_pk_fma_f32 v[100:101], v[100:101], v[174:175], v[148:149] op_sel_hi:[1,0,1]
	v_pk_fma_f32 v[96:97], v[96:97], v[174:175], v[144:145] op_sel_hi:[1,0,1]
	v_pk_fma_f32 v[90:91], v[90:91], v[174:175], v[130:131] op_sel_hi:[1,0,1]
	v_pk_fma_f32 v[86:87], v[86:87], v[174:175], v[126:127] op_sel_hi:[1,0,1]
	v_pk_fma_f32 v[92:93], v[92:93], v[174:175], v[132:133] op_sel_hi:[1,0,1]
	v_pk_fma_f32 v[88:89], v[88:89], v[174:175], v[128:129] op_sel_hi:[1,0,1]
	v_min_f32_e32 v98, 0x40e00000, v98
	v_min_f32_e32 v99, 0x40e00000, v99
	v_min_f32_e32 v100, 0x40e00000, v100
	v_min_f32_e32 v101, 0x40e00000, v101
	v_min_f32_e32 v90, 0x40e00000, v90
	v_min_f32_e32 v91, 0x40e00000, v91
	v_min_f32_e32 v92, 0x40e00000, v92
	v_min_f32_e32 v93, 0x40e00000, v93
	v_pk_mul_f32 v[166:167], v[98:99], v[178:179] op_sel_hi:[1,0]
	v_pk_mul_f32 v[168:169], v[100:101], v[178:179] op_sel_hi:[1,0]
	v_pk_mul_f32 v[170:171], v[90:91], v[178:179] op_sel_hi:[1,0]
	v_pk_mul_f32 v[172:173], v[92:93], v[178:179] op_sel_hi:[1,0]
	v_med3_f32 v94, v94, s74, v223
	v_med3_f32 v95, v95, s74, v223
	v_med3_f32 v96, v96, s74, v223
	v_med3_f32 v97, v97, s74, v223
	v_med3_f32 v86, v86, s74, v223
	v_med3_f32 v87, v87, s74, v223
	v_med3_f32 v88, v88, s74, v223
	v_med3_f32 v89, v89, s74, v223
	v_exp_f32_e32 v166, v166
	v_exp_f32_e32 v167, v167
	v_exp_f32_e32 v168, v168
	v_exp_f32_e32 v169, v169
	v_exp_f32_e32 v170, v170
	v_exp_f32_e32 v171, v171
	v_exp_f32_e32 v172, v172
	v_exp_f32_e32 v173, v173
	v_pk_add_f32 v[94:95], v[94:95], 1.0 op_sel_hi:[1,0]
	v_pk_add_f32 v[96:97], v[96:97], 1.0 op_sel_hi:[1,0]
	v_pk_add_f32 v[86:87], v[86:87], 1.0 op_sel_hi:[1,0]
	v_pk_add_f32 v[88:89], v[88:89], 1.0 op_sel_hi:[1,0]
	v_pk_add_f32 v[166:167], v[166:167], 1.0 op_sel_hi:[1,0]
	v_pk_add_f32 v[168:169], v[168:169], 1.0 op_sel_hi:[1,0]
	v_pk_add_f32 v[170:171], v[170:171], 1.0 op_sel_hi:[1,0]
	v_pk_add_f32 v[172:173], v[172:173], 1.0 op_sel_hi:[1,0]
	v_rcp_f32_e32 v166, v166
	v_rcp_f32_e32 v167, v167
	v_rcp_f32_e32 v168, v168
	v_rcp_f32_e32 v169, v169
	v_rcp_f32_e32 v170, v170
	v_rcp_f32_e32 v171, v171
	v_rcp_f32_e32 v172, v172
	v_rcp_f32_e32 v173, v173
	s_nop 0
	v_pk_mul_f32 v[98:99], v[98:99], v[166:167]
	v_pk_mul_f32 v[100:101], v[100:101], v[168:169]
	v_pk_mul_f32 v[90:91], v[90:91], v[170:171]
	v_pk_mul_f32 v[92:93], v[92:93], v[172:173]
	v_pk_mul_f32 v[94:95], v[94:95], v[98:99]
	v_pk_mul_f32 v[96:97], v[96:97], v[100:101]
	v_pk_mul_f32 v[86:87], v[86:87], v[90:91]
	v_pk_mul_f32 v[88:89], v[88:89], v[92:93]
	v_pk_fma_f32 v[94:95], v[94:95], v[176:177], v[222:223] op_sel_hi:[1,0,0]
	v_pk_fma_f32 v[96:97], v[96:97], v[176:177], v[222:223] op_sel_hi:[1,0,0]
	v_pk_fma_f32 v[86:87], v[86:87], v[176:177], v[222:223] op_sel_hi:[1,0,0]
	v_pk_fma_f32 v[88:89], v[88:89], v[176:177], v[222:223] op_sel_hi:[1,0,0]
	v_med3_f32 v94, v94, s75, v224
	v_med3_f32 v95, v95, s75, v224
	v_med3_f32 v96, v96, s75, v224
	v_med3_f32 v97, v97, s75, v224
	v_med3_f32 v86, v86, s75, v224
	v_med3_f32 v87, v87, s75, v224
	v_med3_f32 v88, v88, s75, v224
	v_med3_f32 v89, v89, s75, v224
	v_perm_b32 v94, v95, v94, s76
	v_perm_b32 v96, v97, v96, s76
	v_perm_b32 v86, v87, v86, s76
	v_perm_b32 v88, v89, v88, s76
	v_perm_b32 v166, v96, v94, s77
	v_perm_b32 v167, v88, v86, s77
	v_add_u32_e32 v86, s4, v102
	v_ashrrev_i32_e32 v87, 31, v86
	v_lshlrev_b64 v[86:87], 11, v[86:87]
	v_lshl_add_u64 v[86:87], s[10:11], 0, v[86:87]
	v_lshl_add_u64 v[86:87], v[86:87], 0, v[4:5]
	v_mov_b32_e32 v94, v166
	v_mov_b32_e32 v95, v167
	global_store_dwordx2 v[86:87], v[94:95], off
.LBB0_971:
	s_or_b64 exec, exec, s[0:1]
	v_or_b32_e32 v86, 48, v150
	v_cmp_lt_i32_e32 vcc, v86, v151
	s_and_saveexec_b64 s[0:1], vcc
	s_cbranch_execz .LBB0_973
	v_mul_f32_e32 v174, 0x3a800000, v155
	v_cvt_f32_i32_e32 v82, v82
	v_cvt_f32_i32_e32 v83, v83
	v_cvt_f32_i32_e32 v84, v84
	v_cvt_f32_i32_e32 v85, v85
	v_cvt_f32_i32_e32 v78, v78
	v_cvt_f32_i32_e32 v79, v79
	v_cvt_f32_i32_e32 v80, v80
	v_cvt_f32_i32_e32 v81, v81
	v_cvt_f32_i32_e32 v74, v74
	v_cvt_f32_i32_e32 v75, v75
	v_cvt_f32_i32_e32 v76, v76
	v_cvt_f32_i32_e32 v77, v77
	v_cvt_f32_i32_e32 v70, v70
	v_cvt_f32_i32_e32 v71, v71
	v_cvt_f32_i32_e32 v72, v72
	v_cvt_f32_i32_e32 v73, v73
	v_pk_fma_f32 v[82:83], v[82:83], v[174:175], v[146:147] op_sel_hi:[1,0,1]
	v_pk_fma_f32 v[78:79], v[78:79], v[174:175], v[142:143] op_sel_hi:[1,0,1]
	v_pk_fma_f32 v[84:85], v[84:85], v[174:175], v[148:149] op_sel_hi:[1,0,1]
	v_pk_fma_f32 v[80:81], v[80:81], v[174:175], v[144:145] op_sel_hi:[1,0,1]
	v_pk_fma_f32 v[74:75], v[74:75], v[174:175], v[130:131] op_sel_hi:[1,0,1]
	v_pk_fma_f32 v[70:71], v[70:71], v[174:175], v[126:127] op_sel_hi:[1,0,1]
	v_pk_fma_f32 v[76:77], v[76:77], v[174:175], v[132:133] op_sel_hi:[1,0,1]
	v_pk_fma_f32 v[72:73], v[72:73], v[174:175], v[128:129] op_sel_hi:[1,0,1]
	v_min_f32_e32 v82, 0x40e00000, v82
	v_min_f32_e32 v83, 0x40e00000, v83
	v_min_f32_e32 v84, 0x40e00000, v84
	v_min_f32_e32 v85, 0x40e00000, v85
	v_min_f32_e32 v74, 0x40e00000, v74
	v_min_f32_e32 v75, 0x40e00000, v75
	v_min_f32_e32 v76, 0x40e00000, v76
	v_min_f32_e32 v77, 0x40e00000, v77
	v_pk_mul_f32 v[166:167], v[82:83], v[178:179] op_sel_hi:[1,0]
	v_pk_mul_f32 v[168:169], v[84:85], v[178:179] op_sel_hi:[1,0]
	v_pk_mul_f32 v[170:171], v[74:75], v[178:179] op_sel_hi:[1,0]
	v_pk_mul_f32 v[172:173], v[76:77], v[178:179] op_sel_hi:[1,0]
	v_med3_f32 v78, v78, s74, v223
	v_med3_f32 v79, v79, s74, v223
	v_med3_f32 v80, v80, s74, v223
	v_med3_f32 v81, v81, s74, v223
	v_med3_f32 v70, v70, s74, v223
	v_med3_f32 v71, v71, s74, v223
	v_med3_f32 v72, v72, s74, v223
	v_med3_f32 v73, v73, s74, v223
	v_exp_f32_e32 v166, v166
	v_exp_f32_e32 v167, v167
	v_exp_f32_e32 v168, v168
	v_exp_f32_e32 v169, v169
	v_exp_f32_e32 v170, v170
	v_exp_f32_e32 v171, v171
	v_exp_f32_e32 v172, v172
	v_exp_f32_e32 v173, v173
	v_pk_add_f32 v[78:79], v[78:79], 1.0 op_sel_hi:[1,0]
	v_pk_add_f32 v[80:81], v[80:81], 1.0 op_sel_hi:[1,0]
	v_pk_add_f32 v[70:71], v[70:71], 1.0 op_sel_hi:[1,0]
	v_pk_add_f32 v[72:73], v[72:73], 1.0 op_sel_hi:[1,0]
	v_pk_add_f32 v[166:167], v[166:167], 1.0 op_sel_hi:[1,0]
	v_pk_add_f32 v[168:169], v[168:169], 1.0 op_sel_hi:[1,0]
	v_pk_add_f32 v[170:171], v[170:171], 1.0 op_sel_hi:[1,0]
	v_pk_add_f32 v[172:173], v[172:173], 1.0 op_sel_hi:[1,0]
	v_rcp_f32_e32 v166, v166
	v_rcp_f32_e32 v167, v167
	v_rcp_f32_e32 v168, v168
	v_rcp_f32_e32 v169, v169
	v_rcp_f32_e32 v170, v170
	v_rcp_f32_e32 v171, v171
	v_rcp_f32_e32 v172, v172
	v_rcp_f32_e32 v173, v173
	s_nop 0
	v_pk_mul_f32 v[82:83], v[82:83], v[166:167]
	v_pk_mul_f32 v[84:85], v[84:85], v[168:169]
	v_pk_mul_f32 v[74:75], v[74:75], v[170:171]
	v_pk_mul_f32 v[76:77], v[76:77], v[172:173]
	v_pk_mul_f32 v[78:79], v[78:79], v[82:83]
	v_pk_mul_f32 v[80:81], v[80:81], v[84:85]
	v_pk_mul_f32 v[70:71], v[70:71], v[74:75]
	v_pk_mul_f32 v[72:73], v[72:73], v[76:77]
	v_pk_fma_f32 v[78:79], v[78:79], v[176:177], v[222:223] op_sel_hi:[1,0,0]
	v_pk_fma_f32 v[80:81], v[80:81], v[176:177], v[222:223] op_sel_hi:[1,0,0]
	v_pk_fma_f32 v[70:71], v[70:71], v[176:177], v[222:223] op_sel_hi:[1,0,0]
	v_pk_fma_f32 v[72:73], v[72:73], v[176:177], v[222:223] op_sel_hi:[1,0,0]
	v_med3_f32 v78, v78, s75, v224
	v_med3_f32 v79, v79, s75, v224
	v_med3_f32 v80, v80, s75, v224
	v_med3_f32 v81, v81, s75, v224
	v_med3_f32 v70, v70, s75, v224
	v_med3_f32 v71, v71, s75, v224
	v_med3_f32 v72, v72, s75, v224
	v_med3_f32 v73, v73, s75, v224
	v_perm_b32 v78, v79, v78, s76
	v_perm_b32 v80, v81, v80, s76
	v_perm_b32 v70, v71, v70, s76
	v_perm_b32 v72, v73, v72, s76
	v_perm_b32 v166, v80, v78, s77
	v_perm_b32 v167, v72, v70, s77
	v_add_u32_e32 v70, s4, v86
	v_ashrrev_i32_e32 v71, 31, v70
	v_lshlrev_b64 v[70:71], 11, v[70:71]
	v_lshl_add_u64 v[70:71], s[10:11], 0, v[70:71]
	v_lshl_add_u64 v[70:71], v[70:71], 0, v[4:5]
	v_mov_b32_e32 v78, v166
	v_mov_b32_e32 v79, v167
	global_store_dwordx2 v[70:71], v[78:79], off
.LBB0_973:
	s_or_b64 exec, exec, s[0:1]
	v_add_u32_e32 v70, 0x80, v150
	v_cmp_lt_i32_e32 vcc, v70, v151
	s_and_saveexec_b64 s[0:1], vcc
	s_cbranch_execz .LBB0_975
	v_mul_f32_e32 v174, 0x3a800000, v154
	v_cvt_f32_i32_e32 v66, v66
	v_cvt_f32_i32_e32 v67, v67
	v_cvt_f32_i32_e32 v68, v68
	v_cvt_f32_i32_e32 v69, v69
	v_cvt_f32_i32_e32 v62, v62
	v_cvt_f32_i32_e32 v63, v63
	v_cvt_f32_i32_e32 v64, v64
	v_cvt_f32_i32_e32 v65, v65
	v_cvt_f32_i32_e32 v58, v58
	v_cvt_f32_i32_e32 v59, v59
	v_cvt_f32_i32_e32 v60, v60
	v_cvt_f32_i32_e32 v61, v61
	v_cvt_f32_i32_e32 v54, v54
	v_cvt_f32_i32_e32 v55, v55
	v_cvt_f32_i32_e32 v56, v56
	v_cvt_f32_i32_e32 v57, v57
	v_pk_fma_f32 v[66:67], v[66:67], v[174:175], v[146:147] op_sel_hi:[1,0,1]
	v_pk_fma_f32 v[62:63], v[62:63], v[174:175], v[142:143] op_sel_hi:[1,0,1]
	v_pk_fma_f32 v[68:69], v[68:69], v[174:175], v[148:149] op_sel_hi:[1,0,1]
	v_pk_fma_f32 v[64:65], v[64:65], v[174:175], v[144:145] op_sel_hi:[1,0,1]
	v_pk_fma_f32 v[58:59], v[58:59], v[174:175], v[130:131] op_sel_hi:[1,0,1]
	v_pk_fma_f32 v[54:55], v[54:55], v[174:175], v[126:127] op_sel_hi:[1,0,1]
	v_pk_fma_f32 v[60:61], v[60:61], v[174:175], v[132:133] op_sel_hi:[1,0,1]
	v_pk_fma_f32 v[56:57], v[56:57], v[174:175], v[128:129] op_sel_hi:[1,0,1]
	v_min_f32_e32 v66, 0x40e00000, v66
	v_min_f32_e32 v67, 0x40e00000, v67
	v_min_f32_e32 v68, 0x40e00000, v68
	v_min_f32_e32 v69, 0x40e00000, v69
	v_min_f32_e32 v58, 0x40e00000, v58
	v_min_f32_e32 v59, 0x40e00000, v59
	v_min_f32_e32 v60, 0x40e00000, v60
	v_min_f32_e32 v61, 0x40e00000, v61
	v_pk_mul_f32 v[166:167], v[66:67], v[178:179] op_sel_hi:[1,0]
	v_pk_mul_f32 v[168:169], v[68:69], v[178:179] op_sel_hi:[1,0]
	v_pk_mul_f32 v[170:171], v[58:59], v[178:179] op_sel_hi:[1,0]
	v_pk_mul_f32 v[172:173], v[60:61], v[178:179] op_sel_hi:[1,0]
	v_med3_f32 v62, v62, s74, v223
	v_med3_f32 v63, v63, s74, v223
	v_med3_f32 v64, v64, s74, v223
	v_med3_f32 v65, v65, s74, v223
	v_med3_f32 v54, v54, s74, v223
	v_med3_f32 v55, v55, s74, v223
	v_med3_f32 v56, v56, s74, v223
	v_med3_f32 v57, v57, s74, v223
	v_exp_f32_e32 v166, v166
	v_exp_f32_e32 v167, v167
	v_exp_f32_e32 v168, v168
	v_exp_f32_e32 v169, v169
	v_exp_f32_e32 v170, v170
	v_exp_f32_e32 v171, v171
	v_exp_f32_e32 v172, v172
	v_exp_f32_e32 v173, v173
	v_pk_add_f32 v[62:63], v[62:63], 1.0 op_sel_hi:[1,0]
	v_pk_add_f32 v[64:65], v[64:65], 1.0 op_sel_hi:[1,0]
	v_pk_add_f32 v[54:55], v[54:55], 1.0 op_sel_hi:[1,0]
	v_pk_add_f32 v[56:57], v[56:57], 1.0 op_sel_hi:[1,0]
	v_pk_add_f32 v[166:167], v[166:167], 1.0 op_sel_hi:[1,0]
	v_pk_add_f32 v[168:169], v[168:169], 1.0 op_sel_hi:[1,0]
	v_pk_add_f32 v[170:171], v[170:171], 1.0 op_sel_hi:[1,0]
	v_pk_add_f32 v[172:173], v[172:173], 1.0 op_sel_hi:[1,0]
	v_rcp_f32_e32 v166, v166
	v_rcp_f32_e32 v167, v167
	v_rcp_f32_e32 v168, v168
	v_rcp_f32_e32 v169, v169
	v_rcp_f32_e32 v170, v170
	v_rcp_f32_e32 v171, v171
	v_rcp_f32_e32 v172, v172
	v_rcp_f32_e32 v173, v173
	s_nop 0
	v_pk_mul_f32 v[66:67], v[66:67], v[166:167]
	v_pk_mul_f32 v[68:69], v[68:69], v[168:169]
	v_pk_mul_f32 v[58:59], v[58:59], v[170:171]
	v_pk_mul_f32 v[60:61], v[60:61], v[172:173]
	v_pk_mul_f32 v[62:63], v[62:63], v[66:67]
	v_pk_mul_f32 v[64:65], v[64:65], v[68:69]
	v_pk_mul_f32 v[54:55], v[54:55], v[58:59]
	v_pk_mul_f32 v[56:57], v[56:57], v[60:61]
	v_pk_fma_f32 v[62:63], v[62:63], v[176:177], v[222:223] op_sel_hi:[1,0,0]
	v_pk_fma_f32 v[64:65], v[64:65], v[176:177], v[222:223] op_sel_hi:[1,0,0]
	v_pk_fma_f32 v[54:55], v[54:55], v[176:177], v[222:223] op_sel_hi:[1,0,0]
	v_pk_fma_f32 v[56:57], v[56:57], v[176:177], v[222:223] op_sel_hi:[1,0,0]
	v_med3_f32 v62, v62, s75, v224
	v_med3_f32 v63, v63, s75, v224
	v_med3_f32 v64, v64, s75, v224
	v_med3_f32 v65, v65, s75, v224
	v_med3_f32 v54, v54, s75, v224
	v_med3_f32 v55, v55, s75, v224
	v_med3_f32 v56, v56, s75, v224
	v_med3_f32 v57, v57, s75, v224
	v_perm_b32 v62, v63, v62, s76
	v_perm_b32 v64, v65, v64, s76
	v_perm_b32 v54, v55, v54, s76
	v_perm_b32 v56, v57, v56, s76
	v_perm_b32 v166, v64, v62, s77
	v_perm_b32 v167, v56, v54, s77
	v_add_u32_e32 v54, s4, v70
	v_ashrrev_i32_e32 v55, 31, v54
	v_lshlrev_b64 v[54:55], 11, v[54:55]
	v_lshl_add_u64 v[54:55], s[10:11], 0, v[54:55]
	v_lshl_add_u64 v[54:55], v[54:55], 0, v[4:5]
	v_mov_b32_e32 v62, v166
	v_mov_b32_e32 v63, v167
	global_store_dwordx2 v[54:55], v[62:63], off
.LBB0_975:
	s_or_b64 exec, exec, s[0:1]
	v_add_u32_e32 v54, 0x90, v150
	v_cmp_lt_i32_e32 vcc, v54, v151
	s_and_saveexec_b64 s[0:1], vcc
	s_cbranch_execz .LBB0_977
	v_mul_f32_e32 v174, 0x3a800000, v153
	v_cvt_f32_i32_e32 v50, v50
	v_cvt_f32_i32_e32 v51, v51
	v_cvt_f32_i32_e32 v52, v52
	v_cvt_f32_i32_e32 v53, v53
	v_cvt_f32_i32_e32 v46, v46
	v_cvt_f32_i32_e32 v47, v47
	v_cvt_f32_i32_e32 v48, v48
	v_cvt_f32_i32_e32 v49, v49
	v_cvt_f32_i32_e32 v42, v42
	v_cvt_f32_i32_e32 v43, v43
	v_cvt_f32_i32_e32 v44, v44
	v_cvt_f32_i32_e32 v45, v45
	v_cvt_f32_i32_e32 v38, v38
	v_cvt_f32_i32_e32 v39, v39
	v_cvt_f32_i32_e32 v40, v40
	v_cvt_f32_i32_e32 v41, v41
	v_pk_fma_f32 v[50:51], v[50:51], v[174:175], v[146:147] op_sel_hi:[1,0,1]
	v_pk_fma_f32 v[46:47], v[46:47], v[174:175], v[142:143] op_sel_hi:[1,0,1]
	v_pk_fma_f32 v[52:53], v[52:53], v[174:175], v[148:149] op_sel_hi:[1,0,1]
	v_pk_fma_f32 v[48:49], v[48:49], v[174:175], v[144:145] op_sel_hi:[1,0,1]
	v_pk_fma_f32 v[42:43], v[42:43], v[174:175], v[130:131] op_sel_hi:[1,0,1]
	v_pk_fma_f32 v[38:39], v[38:39], v[174:175], v[126:127] op_sel_hi:[1,0,1]
	v_pk_fma_f32 v[44:45], v[44:45], v[174:175], v[132:133] op_sel_hi:[1,0,1]
	v_pk_fma_f32 v[40:41], v[40:41], v[174:175], v[128:129] op_sel_hi:[1,0,1]
	v_min_f32_e32 v50, 0x40e00000, v50
	v_min_f32_e32 v51, 0x40e00000, v51
	v_min_f32_e32 v52, 0x40e00000, v52
	v_min_f32_e32 v53, 0x40e00000, v53
	v_min_f32_e32 v42, 0x40e00000, v42
	v_min_f32_e32 v43, 0x40e00000, v43
	v_min_f32_e32 v44, 0x40e00000, v44
	v_min_f32_e32 v45, 0x40e00000, v45
	v_pk_mul_f32 v[166:167], v[50:51], v[178:179] op_sel_hi:[1,0]
	v_pk_mul_f32 v[168:169], v[52:53], v[178:179] op_sel_hi:[1,0]
	v_pk_mul_f32 v[170:171], v[42:43], v[178:179] op_sel_hi:[1,0]
	v_pk_mul_f32 v[172:173], v[44:45], v[178:179] op_sel_hi:[1,0]
	v_med3_f32 v46, v46, s74, v223
	v_med3_f32 v47, v47, s74, v223
	v_med3_f32 v48, v48, s74, v223
	v_med3_f32 v49, v49, s74, v223
	v_med3_f32 v38, v38, s74, v223
	v_med3_f32 v39, v39, s74, v223
	v_med3_f32 v40, v40, s74, v223
	v_med3_f32 v41, v41, s74, v223
	v_exp_f32_e32 v166, v166
	v_exp_f32_e32 v167, v167
	v_exp_f32_e32 v168, v168
	v_exp_f32_e32 v169, v169
	v_exp_f32_e32 v170, v170
	v_exp_f32_e32 v171, v171
	v_exp_f32_e32 v172, v172
	v_exp_f32_e32 v173, v173
	v_pk_add_f32 v[46:47], v[46:47], 1.0 op_sel_hi:[1,0]
	v_pk_add_f32 v[48:49], v[48:49], 1.0 op_sel_hi:[1,0]
	v_pk_add_f32 v[38:39], v[38:39], 1.0 op_sel_hi:[1,0]
	v_pk_add_f32 v[40:41], v[40:41], 1.0 op_sel_hi:[1,0]
	v_pk_add_f32 v[166:167], v[166:167], 1.0 op_sel_hi:[1,0]
	v_pk_add_f32 v[168:169], v[168:169], 1.0 op_sel_hi:[1,0]
	v_pk_add_f32 v[170:171], v[170:171], 1.0 op_sel_hi:[1,0]
	v_pk_add_f32 v[172:173], v[172:173], 1.0 op_sel_hi:[1,0]
	v_rcp_f32_e32 v166, v166
	v_rcp_f32_e32 v167, v167
	v_rcp_f32_e32 v168, v168
	v_rcp_f32_e32 v169, v169
	v_rcp_f32_e32 v170, v170
	v_rcp_f32_e32 v171, v171
	v_rcp_f32_e32 v172, v172
	v_rcp_f32_e32 v173, v173
	s_nop 0
	v_pk_mul_f32 v[50:51], v[50:51], v[166:167]
	v_pk_mul_f32 v[52:53], v[52:53], v[168:169]
	v_pk_mul_f32 v[42:43], v[42:43], v[170:171]
	v_pk_mul_f32 v[44:45], v[44:45], v[172:173]
	v_pk_mul_f32 v[46:47], v[46:47], v[50:51]
	v_pk_mul_f32 v[48:49], v[48:49], v[52:53]
	v_pk_mul_f32 v[38:39], v[38:39], v[42:43]
	v_pk_mul_f32 v[40:41], v[40:41], v[44:45]
	v_pk_fma_f32 v[46:47], v[46:47], v[176:177], v[222:223] op_sel_hi:[1,0,0]
	v_pk_fma_f32 v[48:49], v[48:49], v[176:177], v[222:223] op_sel_hi:[1,0,0]
	v_pk_fma_f32 v[38:39], v[38:39], v[176:177], v[222:223] op_sel_hi:[1,0,0]
	v_pk_fma_f32 v[40:41], v[40:41], v[176:177], v[222:223] op_sel_hi:[1,0,0]
	v_med3_f32 v46, v46, s75, v224
	v_med3_f32 v47, v47, s75, v224
	v_med3_f32 v48, v48, s75, v224
	v_med3_f32 v49, v49, s75, v224
	v_med3_f32 v38, v38, s75, v224
	v_med3_f32 v39, v39, s75, v224
	v_med3_f32 v40, v40, s75, v224
	v_med3_f32 v41, v41, s75, v224
	v_perm_b32 v46, v47, v46, s76
	v_perm_b32 v48, v49, v48, s76
	v_perm_b32 v38, v39, v38, s76
	v_perm_b32 v40, v41, v40, s76
	v_perm_b32 v166, v48, v46, s77
	v_perm_b32 v167, v40, v38, s77
	v_add_u32_e32 v38, s4, v54
	v_ashrrev_i32_e32 v39, 31, v38
	v_lshlrev_b64 v[38:39], 11, v[38:39]
	v_lshl_add_u64 v[38:39], s[10:11], 0, v[38:39]
	v_lshl_add_u64 v[38:39], v[38:39], 0, v[4:5]
	v_mov_b32_e32 v46, v166
	v_mov_b32_e32 v47, v167
	global_store_dwordx2 v[38:39], v[46:47], off
.LBB0_977:
	s_or_b64 exec, exec, s[0:1]
	v_add_u32_e32 v38, 0xa0, v150
	v_cmp_lt_i32_e32 vcc, v38, v151
	s_and_saveexec_b64 s[0:1], vcc
	s_cbranch_execz .LBB0_979
	v_mul_f32_e32 v174, 0x3a800000, v152
	v_cvt_f32_i32_e32 v34, v34
	v_cvt_f32_i32_e32 v35, v35
	v_cvt_f32_i32_e32 v36, v36
	v_cvt_f32_i32_e32 v37, v37
	v_cvt_f32_i32_e32 v30, v30
	v_cvt_f32_i32_e32 v31, v31
	v_cvt_f32_i32_e32 v32, v32
	v_cvt_f32_i32_e32 v33, v33
	v_cvt_f32_i32_e32 v26, v26
	v_cvt_f32_i32_e32 v27, v27
	v_cvt_f32_i32_e32 v28, v28
	v_cvt_f32_i32_e32 v29, v29
	v_cvt_f32_i32_e32 v22, v22
	v_cvt_f32_i32_e32 v23, v23
	v_cvt_f32_i32_e32 v24, v24
	v_cvt_f32_i32_e32 v25, v25
	v_pk_fma_f32 v[34:35], v[34:35], v[174:175], v[146:147] op_sel_hi:[1,0,1]
	v_pk_fma_f32 v[30:31], v[30:31], v[174:175], v[142:143] op_sel_hi:[1,0,1]
	v_pk_fma_f32 v[36:37], v[36:37], v[174:175], v[148:149] op_sel_hi:[1,0,1]
	v_pk_fma_f32 v[32:33], v[32:33], v[174:175], v[144:145] op_sel_hi:[1,0,1]
	v_pk_fma_f32 v[26:27], v[26:27], v[174:175], v[130:131] op_sel_hi:[1,0,1]
	v_pk_fma_f32 v[22:23], v[22:23], v[174:175], v[126:127] op_sel_hi:[1,0,1]
	v_pk_fma_f32 v[28:29], v[28:29], v[174:175], v[132:133] op_sel_hi:[1,0,1]
	v_pk_fma_f32 v[24:25], v[24:25], v[174:175], v[128:129] op_sel_hi:[1,0,1]
	v_min_f32_e32 v34, 0x40e00000, v34
	v_min_f32_e32 v35, 0x40e00000, v35
	v_min_f32_e32 v36, 0x40e00000, v36
	v_min_f32_e32 v37, 0x40e00000, v37
	v_min_f32_e32 v26, 0x40e00000, v26
	v_min_f32_e32 v27, 0x40e00000, v27
	v_min_f32_e32 v28, 0x40e00000, v28
	v_min_f32_e32 v29, 0x40e00000, v29
	v_pk_mul_f32 v[166:167], v[34:35], v[178:179] op_sel_hi:[1,0]
	v_pk_mul_f32 v[168:169], v[36:37], v[178:179] op_sel_hi:[1,0]
	v_pk_mul_f32 v[170:171], v[26:27], v[178:179] op_sel_hi:[1,0]
	v_pk_mul_f32 v[172:173], v[28:29], v[178:179] op_sel_hi:[1,0]
	v_med3_f32 v30, v30, s74, v223
	v_med3_f32 v31, v31, s74, v223
	v_med3_f32 v32, v32, s74, v223
	v_med3_f32 v33, v33, s74, v223
	v_med3_f32 v22, v22, s74, v223
	v_med3_f32 v23, v23, s74, v223
	v_med3_f32 v24, v24, s74, v223
	v_med3_f32 v25, v25, s74, v223
	v_exp_f32_e32 v166, v166
	v_exp_f32_e32 v167, v167
	v_exp_f32_e32 v168, v168
	v_exp_f32_e32 v169, v169
	v_exp_f32_e32 v170, v170
	v_exp_f32_e32 v171, v171
	v_exp_f32_e32 v172, v172
	v_exp_f32_e32 v173, v173
	v_pk_add_f32 v[30:31], v[30:31], 1.0 op_sel_hi:[1,0]
	v_pk_add_f32 v[32:33], v[32:33], 1.0 op_sel_hi:[1,0]
	v_pk_add_f32 v[22:23], v[22:23], 1.0 op_sel_hi:[1,0]
	v_pk_add_f32 v[24:25], v[24:25], 1.0 op_sel_hi:[1,0]
	v_pk_add_f32 v[166:167], v[166:167], 1.0 op_sel_hi:[1,0]
	v_pk_add_f32 v[168:169], v[168:169], 1.0 op_sel_hi:[1,0]
	v_pk_add_f32 v[170:171], v[170:171], 1.0 op_sel_hi:[1,0]
	v_pk_add_f32 v[172:173], v[172:173], 1.0 op_sel_hi:[1,0]
	v_rcp_f32_e32 v166, v166
	v_rcp_f32_e32 v167, v167
	v_rcp_f32_e32 v168, v168
	v_rcp_f32_e32 v169, v169
	v_rcp_f32_e32 v170, v170
	v_rcp_f32_e32 v171, v171
	v_rcp_f32_e32 v172, v172
	v_rcp_f32_e32 v173, v173
	s_nop 0
	v_pk_mul_f32 v[34:35], v[34:35], v[166:167]
	v_pk_mul_f32 v[36:37], v[36:37], v[168:169]
	v_pk_mul_f32 v[26:27], v[26:27], v[170:171]
	v_pk_mul_f32 v[28:29], v[28:29], v[172:173]
	v_pk_mul_f32 v[30:31], v[30:31], v[34:35]
	v_pk_mul_f32 v[32:33], v[32:33], v[36:37]
	v_pk_mul_f32 v[22:23], v[22:23], v[26:27]
	v_pk_mul_f32 v[24:25], v[24:25], v[28:29]
	v_pk_fma_f32 v[30:31], v[30:31], v[176:177], v[222:223] op_sel_hi:[1,0,0]
	v_pk_fma_f32 v[32:33], v[32:33], v[176:177], v[222:223] op_sel_hi:[1,0,0]
	v_pk_fma_f32 v[22:23], v[22:23], v[176:177], v[222:223] op_sel_hi:[1,0,0]
	v_pk_fma_f32 v[24:25], v[24:25], v[176:177], v[222:223] op_sel_hi:[1,0,0]
	v_med3_f32 v30, v30, s75, v224
	v_med3_f32 v31, v31, s75, v224
	v_med3_f32 v32, v32, s75, v224
	v_med3_f32 v33, v33, s75, v224
	v_med3_f32 v22, v22, s75, v224
	v_med3_f32 v23, v23, s75, v224
	v_med3_f32 v24, v24, s75, v224
	v_med3_f32 v25, v25, s75, v224
	v_perm_b32 v30, v31, v30, s76
	v_perm_b32 v32, v33, v32, s76
	v_perm_b32 v22, v23, v22, s76
	v_perm_b32 v24, v25, v24, s76
	v_perm_b32 v166, v32, v30, s77
	v_perm_b32 v167, v24, v22, s77
	v_add_u32_e32 v22, s4, v38
	v_ashrrev_i32_e32 v23, 31, v22
	v_lshlrev_b64 v[22:23], 11, v[22:23]
	v_lshl_add_u64 v[22:23], s[10:11], 0, v[22:23]
	v_lshl_add_u64 v[22:23], v[22:23], 0, v[4:5]
	v_mov_b32_e32 v30, v166
	v_mov_b32_e32 v31, v167
	global_store_dwordx2 v[22:23], v[30:31], off
.LBB0_979:
	s_or_b64 exec, exec, s[0:1]
	v_add_u32_e32 v22, 0xb0, v150
	v_cmp_lt_i32_e32 vcc, v22, v151
	s_and_saveexec_b64 s[0:1], vcc
	s_cbranch_execz .LBB0_981
	v_mul_f32_e32 v174, 0x3a800000, v3
	v_cvt_f32_i32_e32 v18, v18
	v_cvt_f32_i32_e32 v19, v19
	v_cvt_f32_i32_e32 v20, v20
	v_cvt_f32_i32_e32 v21, v21
	v_cvt_f32_i32_e32 v14, v14
	v_cvt_f32_i32_e32 v15, v15
	v_cvt_f32_i32_e32 v16, v16
	v_cvt_f32_i32_e32 v17, v17
	v_cvt_f32_i32_e32 v10, v10
	v_cvt_f32_i32_e32 v11, v11
	v_cvt_f32_i32_e32 v12, v12
	v_cvt_f32_i32_e32 v13, v13
	v_cvt_f32_i32_e32 v6, v6
	v_cvt_f32_i32_e32 v7, v7
	v_cvt_f32_i32_e32 v8, v8
	v_cvt_f32_i32_e32 v9, v9
	v_pk_fma_f32 v[18:19], v[18:19], v[174:175], v[146:147] op_sel_hi:[1,0,1]
	v_pk_fma_f32 v[14:15], v[14:15], v[174:175], v[142:143] op_sel_hi:[1,0,1]
	v_pk_fma_f32 v[20:21], v[20:21], v[174:175], v[148:149] op_sel_hi:[1,0,1]
	v_pk_fma_f32 v[16:17], v[16:17], v[174:175], v[144:145] op_sel_hi:[1,0,1]
	v_pk_fma_f32 v[10:11], v[10:11], v[174:175], v[130:131] op_sel_hi:[1,0,1]
	v_pk_fma_f32 v[6:7], v[6:7], v[174:175], v[126:127] op_sel_hi:[1,0,1]
	v_pk_fma_f32 v[12:13], v[12:13], v[174:175], v[132:133] op_sel_hi:[1,0,1]
	v_pk_fma_f32 v[8:9], v[8:9], v[174:175], v[128:129] op_sel_hi:[1,0,1]
	v_min_f32_e32 v18, 0x40e00000, v18
	v_min_f32_e32 v19, 0x40e00000, v19
	v_min_f32_e32 v20, 0x40e00000, v20
	v_min_f32_e32 v21, 0x40e00000, v21
	v_min_f32_e32 v10, 0x40e00000, v10
	v_min_f32_e32 v11, 0x40e00000, v11
	v_min_f32_e32 v12, 0x40e00000, v12
	v_min_f32_e32 v13, 0x40e00000, v13
	v_pk_mul_f32 v[166:167], v[18:19], v[178:179] op_sel_hi:[1,0]
	v_pk_mul_f32 v[168:169], v[20:21], v[178:179] op_sel_hi:[1,0]
	v_pk_mul_f32 v[170:171], v[10:11], v[178:179] op_sel_hi:[1,0]
	v_pk_mul_f32 v[172:173], v[12:13], v[178:179] op_sel_hi:[1,0]
	v_med3_f32 v14, v14, s74, v223
	v_med3_f32 v15, v15, s74, v223
	v_med3_f32 v16, v16, s74, v223
	v_med3_f32 v17, v17, s74, v223
	v_med3_f32 v6, v6, s74, v223
	v_med3_f32 v7, v7, s74, v223
	v_med3_f32 v8, v8, s74, v223
	v_med3_f32 v9, v9, s74, v223
	v_exp_f32_e32 v166, v166
	v_exp_f32_e32 v167, v167
	v_exp_f32_e32 v168, v168
	v_exp_f32_e32 v169, v169
	v_exp_f32_e32 v170, v170
	v_exp_f32_e32 v171, v171
	v_exp_f32_e32 v172, v172
	v_exp_f32_e32 v173, v173
	v_pk_add_f32 v[14:15], v[14:15], 1.0 op_sel_hi:[1,0]
	v_pk_add_f32 v[16:17], v[16:17], 1.0 op_sel_hi:[1,0]
	v_pk_add_f32 v[6:7], v[6:7], 1.0 op_sel_hi:[1,0]
	v_pk_add_f32 v[8:9], v[8:9], 1.0 op_sel_hi:[1,0]
	v_pk_add_f32 v[166:167], v[166:167], 1.0 op_sel_hi:[1,0]
	v_pk_add_f32 v[168:169], v[168:169], 1.0 op_sel_hi:[1,0]
	v_pk_add_f32 v[170:171], v[170:171], 1.0 op_sel_hi:[1,0]
	v_pk_add_f32 v[172:173], v[172:173], 1.0 op_sel_hi:[1,0]
	v_rcp_f32_e32 v166, v166
	v_rcp_f32_e32 v167, v167
	v_rcp_f32_e32 v168, v168
	v_rcp_f32_e32 v169, v169
	v_rcp_f32_e32 v170, v170
	v_rcp_f32_e32 v171, v171
	v_rcp_f32_e32 v172, v172
	v_rcp_f32_e32 v173, v173
	s_nop 0
	v_pk_mul_f32 v[18:19], v[18:19], v[166:167]
	v_pk_mul_f32 v[20:21], v[20:21], v[168:169]
	v_pk_mul_f32 v[10:11], v[10:11], v[170:171]
	v_pk_mul_f32 v[12:13], v[12:13], v[172:173]
	v_pk_mul_f32 v[14:15], v[14:15], v[18:19]
	v_pk_mul_f32 v[16:17], v[16:17], v[20:21]
	v_pk_mul_f32 v[6:7], v[6:7], v[10:11]
	v_pk_mul_f32 v[8:9], v[8:9], v[12:13]
	v_pk_fma_f32 v[14:15], v[14:15], v[176:177], v[222:223] op_sel_hi:[1,0,0]
	v_pk_fma_f32 v[16:17], v[16:17], v[176:177], v[222:223] op_sel_hi:[1,0,0]
	v_pk_fma_f32 v[6:7], v[6:7], v[176:177], v[222:223] op_sel_hi:[1,0,0]
	v_pk_fma_f32 v[8:9], v[8:9], v[176:177], v[222:223] op_sel_hi:[1,0,0]
	v_med3_f32 v14, v14, s75, v224
	v_med3_f32 v15, v15, s75, v224
	v_med3_f32 v16, v16, s75, v224
	v_med3_f32 v17, v17, s75, v224
	v_med3_f32 v6, v6, s75, v224
	v_med3_f32 v7, v7, s75, v224
	v_med3_f32 v8, v8, s75, v224
	v_med3_f32 v9, v9, s75, v224
	v_perm_b32 v14, v15, v14, s76
	v_perm_b32 v16, v17, v16, s76
	v_perm_b32 v6, v7, v6, s76
	v_perm_b32 v8, v9, v8, s76
	v_perm_b32 v166, v16, v14, s77
	v_perm_b32 v167, v8, v6, s77
	v_add_u32_e32 v6, s4, v22
	v_ashrrev_i32_e32 v7, 31, v6
	v_lshlrev_b64 v[6:7], 11, v[6:7]
	v_lshl_add_u64 v[6:7], s[10:11], 0, v[6:7]
	v_lshl_add_u64 v[4:5], v[6:7], 0, v[4:5]
	v_mov_b32_e32 v14, v166
	v_mov_b32_e32 v15, v167
	global_store_dwordx2 v[4:5], v[14:15], off
